# stack11
# baseline (speedup 1.0000x reference)
.LBB3_58:
	s_add_i32 s4, s43, s33
	s_add_i32 s4, s4, 20
	s_ashr_i32 s5, s4, 31
	ds_read_b128 v[2:5], v102
	ds_read_b128 v[6:9], v102 offset:8192
	s_lshl_b64 s[4:5], s[4:5], 16
	s_add_u32 s4, s6, s4
	s_addc_u32 s5, s7, s5
	v_mov_b32_e32 v103, 0
	v_lshl_add_u64 v[10:11], s[4:5], 0, v[102:103]
	s_waitcnt lgkmcnt(1)
	global_store_dwordx4 v102, v[2:5], s[4:5] sc1
	v_add_co_u32_e32 v12, vcc, 0x2000, v10
	ds_read_b128 v[2:5], v102 offset:16384
	s_nop 0
	v_addc_co_u32_e32 v13, vcc, 0, v11, vcc
	s_waitcnt lgkmcnt(1)
	global_store_dwordx4 v[12:13], v[6:9], off sc1
	ds_read_b128 v[6:9], v102 offset:24576
	v_lshlrev_b32_e32 v0, 4, v1
	s_waitcnt lgkmcnt(1)
	global_store_dwordx4 v0, v[2:5], s[4:5] sc1
	ds_read_b128 v[0:3], v102 offset:32768
	s_nop 0
	v_add_co_u32_e32 v4, vcc, 0x6000, v10
	s_nop 1
	v_addc_co_u32_e32 v5, vcc, 0, v11, vcc
	s_waitcnt lgkmcnt(1)
	global_store_dwordx4 v[4:5], v[6:9], off sc1
	ds_read_b128 v[4:7], v102 offset:40960
	s_nop 0
	v_lshlrev_b32_e32 v8, 4, v165
	s_waitcnt lgkmcnt(1)
	global_store_dwordx4 v8, v[0:3], s[4:5] sc1
	v_add_co_u32_e32 v8, vcc, 0xa000, v10
	ds_read_b128 v[0:3], v102 offset:49152
	s_nop 0
	v_addc_co_u32_e32 v9, vcc, 0, v11, vcc
	s_waitcnt lgkmcnt(1)
	global_store_dwordx4 v[8:9], v[4:7], off sc1
	ds_read_b128 v[4:7], v102 offset:57344
	v_lshlrev_b32_e32 v8, 4, v232
	s_waitcnt lgkmcnt(1)
	global_store_dwordx4 v8, v[0:3], s[4:5] sc1
	s_nop 1
	v_add_co_u32_e32 v0, vcc, 0xe000, v10
	s_nop 1
	v_addc_co_u32_e32 v1, vcc, 0, v11, vcc
	s_waitcnt lgkmcnt(0)
	global_store_dwordx4 v[0:1], v[4:7], off sc1
	s_and_saveexec_b64 s[4:5], s[2:3]
	s_cbranch_execz .LBB3_60
	s_lshl_b32 s2, s33, 2
	v_mov_b32_e32 v0, s2
	global_store_dword v0, v230, s[0:1] offset:384
